# expert weight conversion fully hosted in the grid barriers: waves 1-7 convert two 64x64 tiles per barrier; attention phase untouched
# speedup vs baseline: 1.0704x; 1.0057x over previous
.LBB0_11:
	s_or_b64 exec, exec, s[4:5]
	s_load_dwordx16 s[4:19], s[0:1], 0x40
	s_lshl_b32 s26, s74, 3
	s_lshl_b32 s0, s96, 3
	s_mov_b32 s99, 0
	v_writelane_b32 v239, s62, 44
	v_writelane_b32 v239, s63, 45
	s_cmp_lt_i32 s64, 1
	s_waitcnt lgkmcnt(0)
	v_writelane_b32 v239, s4, 7
	s_nop 1
	v_writelane_b32 v239, s5, 8
	v_writelane_b32 v239, s6, 9
	v_writelane_b32 v239, s7, 10
	v_writelane_b32 v239, s8, 11
	v_writelane_b32 v239, s9, 12
	v_writelane_b32 v239, s10, 13
	v_writelane_b32 v239, s11, 14
	v_writelane_b32 v239, s12, 15
	v_writelane_b32 v239, s13, 16
	v_writelane_b32 v239, s14, 17
	v_writelane_b32 v239, s15, 18
	v_writelane_b32 v239, s16, 19
	v_writelane_b32 v239, s17, 20
	v_writelane_b32 v239, s18, 21
	v_writelane_b32 v239, s19, 22
	v_writelane_b32 v239, s0, 23
	s_cselect_b64 s[0:1], -1, 0
	s_cmp_gt_i32 s65, 0
	s_cselect_b64 s[2:3], -1, 0
	s_and_b64 s[4:5], s[0:1], s[2:3]
	s_andn2_b64 vcc, exec, s[4:5]
	s_cbranch_vccnz .LBB0_54
	v_mov_b32_e32 v2, v0
	s_mov_b32 s0, 0x10000
	v_mul_lo_u32 v1, v2, s74
	v_add_u32_e32 v1, s96, v1
	v_readfirstlane_b32 s2, v2
	v_cmp_gt_i32_e32 vcc, s0, v1
	s_and_saveexec_b64 s[6:7], vcc
	s_cbranch_execz .LBB0_15
	v_and_b32_e32 v4, 31, v1
	s_mov_b32 s0, 0x979a371
	v_cvt_f64_u32_e32 v[4:5], v4
	s_mov_b32 s1, 0xbfda934f
	v_mul_f64 v[4:5], v[4:5], s[0:1]
	v_rndne_f64_e32 v[6:7], v[4:5]
	s_mov_b32 s0, 0x3b39803f
	v_add_f64 v[8:9], v[4:5], -v[6:7]
	s_mov_b32 s1, 0x3c7abc9e
	v_mul_f64 v[10:11], v[8:9], s[0:1]
	s_mov_b32 s0, 0xfefa39ef
	s_mov_b32 s1, 0x3fe62e42
	v_fmac_f64_e32 v[10:11], s[0:1], v[8:9]
	s_mov_b32 s0, 0x6a5dcb37
	v_mov_b32_e32 v8, 0xfca7ab0c
	v_mov_b32_e32 v9, 0x3e928af3
	s_mov_b32 s1, 0x3e5ade15
	v_fmac_f64_e32 v[8:9], s[0:1], v[10:11]
	v_mov_b32_e32 v12, 0x623fde64
	v_mov_b32_e32 v13, 0x3ec71dee
	v_fmac_f64_e32 v[12:13], v[10:11], v[8:9]
	v_mov_b32_e32 v8, 0x7c89e6b0
	v_mov_b32_e32 v9, 0x3efa0199
	v_fmac_f64_e32 v[8:9], v[10:11], v[12:13]
	v_mov_b32_e32 v12, 0x14761f6e
	v_mov_b32_e32 v13, 0x3f2a01a0
	v_fmac_f64_e32 v[12:13], v[10:11], v[8:9]
	v_mov_b32_e32 v8, 0x1852b7b0
	v_mov_b32_e32 v9, 0x3f56c16c
	v_fmac_f64_e32 v[8:9], v[10:11], v[12:13]
	v_mov_b32_e32 v12, 0x11122322
	v_mov_b32_e32 v13, 0x3f811111
	v_fmac_f64_e32 v[12:13], v[10:11], v[8:9]
	v_mov_b32_e32 v8, 0x555502a1
	v_mov_b32_e32 v9, 0x3fa55555
	v_fmac_f64_e32 v[8:9], v[10:11], v[12:13]
	v_mov_b32_e32 v12, 0x55555511
	v_mov_b32_e32 v13, 0x3fc55555
	v_fmac_f64_e32 v[12:13], v[10:11], v[8:9]
	v_mov_b32_e32 v8, 11
	v_mov_b32_e32 v9, 0x3fe00000
	s_mov_b32 s0, 0
	v_fmac_f64_e32 v[8:9], v[10:11], v[12:13]
	s_mov_b32 s1, 0x40900000
	v_fma_f64 v[8:9], v[10:11], v[8:9], 1.0
	v_cmp_nlt_f64_e32 vcc, s[0:1], v[4:5]
	s_mov_b32 s0, 0
	v_fma_f64 v[8:9], v[10:11], v[8:9], 1.0
	v_cvt_i32_f64_e32 v6, v[6:7]
	s_mov_b32 s1, 0xc090cc00
	s_add_u32 s8, s62, 0x100000
	v_ldexp_f64 v[6:7], v[8:9], v6
	v_mov_b32_e32 v8, 0x7ff00000
	v_cmp_ngt_f64_e64 s[0:1], s[0:1], v[4:5]
	s_addc_u32 s9, s63, 0
	v_cndmask_b32_e32 v7, v8, v7, vcc
	s_and_b64 vcc, s[0:1], vcc
	s_mov_b32 s10, 0x6dc9c883
	s_mov_b32 s12, 0x54442d18
	s_lshl_b32 s3, s74, 9
	v_and_b32_e32 v3, 3, v1
	v_cndmask_b32_e64 v5, 0, v7, s[0:1]
	v_cndmask_b32_e32 v4, 0, v6, vcc
	v_bfe_u32 v6, v1, 3, 2
	v_lshlrev_b32_e32 v7, 13, v1
	s_lshl_b32 s15, s74, 22
	s_mov_b64 s[0:1], 0
	s_mov_b32 s11, 0x3fc45f30
	s_mov_b32 s13, 0xc01921fb
	s_mov_b32 s14, 0x3d000000
	s_mov_b32 s16, 0x3fffffc
	s_mov_b32 s17, 0xffff

.Lhw_seam0:
	s_mov_b64 exec, -1
	v_readlane_b32 s2, v239, 0
	s_lshr_b32 s2, s2, 6
	s_sub_i32 s2, s2, 1
	s_mul_i32 s2, s2, 2
	s_mul_i32 s9, s99, 14
	s_add_i32 s2, s2, s9
	s_add_i32 s2, s2, 0
	s_mul_i32 s2, s2, s74
	v_readlane_b32 s9, v239, 23
	s_lshr_b32 s9, s9, 3
	s_add_i32 s2, s2, s9
	s_cmp_gt_u32 s2, 24575
	s_cbranch_scc1 .Lhw_seam0_done
	v_mbcnt_lo_u32_b32 v178, -1, 0
	v_mbcnt_hi_u32_b32 v178, -1, v178
	v_and_b32_e32 v179, 60, v178
	v_lshlrev_b32_e32 v179, 10, v179
	v_and_b32_e32 v180, 3, v178
	v_lshl_or_b32 v179, v180, 4, v179
	v_add_u32_e32 v180, 0x400, v179
	v_add_u32_e32 v181, 0x800, v179
	v_add_u32_e32 v190, 0xc00, v179
	v_lshlrev_b32_e32 v178, 2, v178
	s_cmp_lt_u32 s2, 16384
	s_cbranch_scc0 .Lhw_dn_s0_0
	s_lshr_b32 s9, s2, 9
	s_bfe_u32 s32, s2, 0x40005
	s_and_b32 s53, s2, 31
	s_lshl_b32 s69, s9, 23
	s_lshl_b32 s100, s32, 19
	s_add_i32 s69, s69, s100
	s_lshl_b32 s100, s53, 8
	s_add_i32 s69, s69, s100
	s_lshl_b32 s98, s9, 11
	s_bfe_u32 s100, s53, 0x30001
	s_lshl_b32 s100, s100, 8
	s_add_i32 s98, s98, s100
	s_lshr_b32 s100, s53, 4
	s_lshl_b32 s100, s100, 7
	s_add_i32 s98, s98, s100
	s_and_b32 s100, s53, 1
	s_lshl_b32 s100, s100, 6
	s_add_i32 s98, s98, s100
	s_lshl_b32 s98, s98, 10
	s_lshl_b32 s100, s32, 6
	s_add_i32 s98, s98, s100
	s_add_i32 s98, s98, 0x2000000
	v_readlane_b32 s82, v239, 11
	v_readlane_b32 s83, v239, 12
	s_movk_i32 s89, 8192
	s_branch .Lhw_go_s0_0
.Lhw_dn_s0_0:
	s_sub_i32 s2, s2, 16384
	s_lshr_b32 s9, s2, 8
	s_bfe_u32 s32, s2, 0x40004
	s_and_b32 s53, s2, 15
	s_lshl_b32 s69, s9, 22
	s_lshl_b32 s100, s32, 18
	s_add_i32 s69, s69, s100
	s_lshl_b32 s100, s53, 8
	s_add_i32 s69, s69, s100
	s_lshl_b32 s98, s9, 20
	s_lshl_b32 s100, s53, 16
	s_add_i32 s98, s98, s100
	s_lshl_b32 s100, s32, 6
	s_add_i32 s98, s98, s100
	s_add_i32 s98, s98, 0x6000000
	v_readlane_b32 s82, v239, 15
	v_readlane_b32 s83, v239, 16
	s_movk_i32 s89, 4096
.Lhw_go_s0_0:
	s_add_u32 s100, s82, s69
	s_addc_u32 s101, s83, 0
	v_readlane_b32 s82, v239, 44
	v_readlane_b32 s83, v239, 45
	s_add_u32 s82, s82, s98
	s_addc_u32 s83, s83, 0
	global_load_dword v34, v178, s[100:101] nt
	s_add_u32 s100, s100, s89
	s_addc_u32 s101, s101, 0
	global_load_dword v35, v178, s[100:101] nt
	s_add_u32 s100, s100, s89
	s_addc_u32 s101, s101, 0
	global_load_dword v36, v178, s[100:101] nt
	s_add_u32 s100, s100, s89
	s_addc_u32 s101, s101, 0
	global_load_dword v37, v178, s[100:101] nt
	s_add_u32 s100, s100, s89
	s_addc_u32 s101, s101, 0
	global_load_dword v38, v178, s[100:101] nt
	s_add_u32 s100, s100, s89
	s_addc_u32 s101, s101, 0
	global_load_dword v39, v178, s[100:101] nt
	s_add_u32 s100, s100, s89
	s_addc_u32 s101, s101, 0
	global_load_dword v40, v178, s[100:101] nt
	s_add_u32 s100, s100, s89
	s_addc_u32 s101, s101, 0
	global_load_dword v41, v178, s[100:101] nt
	s_add_u32 s100, s100, s89
	s_addc_u32 s101, s101, 0
	global_load_dword v42, v178, s[100:101] nt
	s_add_u32 s100, s100, s89
	s_addc_u32 s101, s101, 0
	global_load_dword v43, v178, s[100:101] nt
	s_add_u32 s100, s100, s89
	s_addc_u32 s101, s101, 0
	global_load_dword v44, v178, s[100:101] nt
	s_add_u32 s100, s100, s89
	s_addc_u32 s101, s101, 0
	global_load_dword v45, v178, s[100:101] nt
	s_add_u32 s100, s100, s89
	s_addc_u32 s101, s101, 0
	global_load_dword v46, v178, s[100:101] nt
	s_add_u32 s100, s100, s89
	s_addc_u32 s101, s101, 0
	global_load_dword v47, v178, s[100:101] nt
	s_add_u32 s100, s100, s89
	s_addc_u32 s101, s101, 0
	global_load_dword v48, v178, s[100:101] nt
	s_add_u32 s100, s100, s89
	s_addc_u32 s101, s101, 0
	global_load_dword v49, v178, s[100:101] nt
	s_add_u32 s100, s100, s89
	s_addc_u32 s101, s101, 0
	global_load_dword v50, v178, s[100:101] nt
	s_add_u32 s100, s100, s89
	s_addc_u32 s101, s101, 0
	global_load_dword v51, v178, s[100:101] nt
	s_add_u32 s100, s100, s89
	s_addc_u32 s101, s101, 0
	global_load_dword v52, v178, s[100:101] nt
	s_add_u32 s100, s100, s89
	s_addc_u32 s101, s101, 0
	global_load_dword v53, v178, s[100:101] nt
	s_add_u32 s100, s100, s89
	s_addc_u32 s101, s101, 0
	global_load_dword v54, v178, s[100:101] nt
	s_add_u32 s100, s100, s89
	s_addc_u32 s101, s101, 0
	global_load_dword v55, v178, s[100:101] nt
	s_add_u32 s100, s100, s89
	s_addc_u32 s101, s101, 0
	global_load_dword v56, v178, s[100:101] nt
	s_add_u32 s100, s100, s89
	s_addc_u32 s101, s101, 0
	global_load_dword v57, v178, s[100:101] nt
	s_add_u32 s100, s100, s89
	s_addc_u32 s101, s101, 0
	global_load_dword v58, v178, s[100:101] nt
	s_add_u32 s100, s100, s89
	s_addc_u32 s101, s101, 0
	global_load_dword v59, v178, s[100:101] nt
	s_add_u32 s100, s100, s89
	s_addc_u32 s101, s101, 0
	global_load_dword v60, v178, s[100:101] nt
	s_add_u32 s100, s100, s89
	s_addc_u32 s101, s101, 0
	global_load_dword v61, v178, s[100:101] nt
	s_add_u32 s100, s100, s89
	s_addc_u32 s101, s101, 0
	global_load_dword v62, v178, s[100:101] nt
	s_add_u32 s100, s100, s89
	s_addc_u32 s101, s101, 0
	global_load_dword v63, v178, s[100:101] nt
	s_add_u32 s100, s100, s89
	s_addc_u32 s101, s101, 0
	global_load_dword v64, v178, s[100:101] nt
	s_add_u32 s100, s100, s89
	s_addc_u32 s101, s101, 0
	global_load_dword v65, v178, s[100:101] nt
	s_add_u32 s100, s100, s89
	s_addc_u32 s101, s101, 0
	global_load_dword v66, v178, s[100:101] nt
	s_add_u32 s100, s100, s89
	s_addc_u32 s101, s101, 0
	global_load_dword v67, v178, s[100:101] nt
	s_add_u32 s100, s100, s89
	s_addc_u32 s101, s101, 0
	global_load_dword v68, v178, s[100:101] nt
	s_add_u32 s100, s100, s89
	s_addc_u32 s101, s101, 0
	global_load_dword v69, v178, s[100:101] nt
	s_add_u32 s100, s100, s89
	s_addc_u32 s101, s101, 0
	global_load_dword v70, v178, s[100:101] nt
	s_add_u32 s100, s100, s89
	s_addc_u32 s101, s101, 0
	global_load_dword v71, v178, s[100:101] nt
	s_add_u32 s100, s100, s89
	s_addc_u32 s101, s101, 0
	global_load_dword v72, v178, s[100:101] nt
	s_add_u32 s100, s100, s89
	s_addc_u32 s101, s101, 0
	global_load_dword v73, v178, s[100:101] nt
	s_add_u32 s100, s100, s89
	s_addc_u32 s101, s101, 0
	global_load_dword v74, v178, s[100:101] nt
	s_add_u32 s100, s100, s89
	s_addc_u32 s101, s101, 0
	global_load_dword v75, v178, s[100:101] nt
	s_add_u32 s100, s100, s89
	s_addc_u32 s101, s101, 0
	global_load_dword v76, v178, s[100:101] nt
	s_add_u32 s100, s100, s89
	s_addc_u32 s101, s101, 0
	global_load_dword v77, v178, s[100:101] nt
	s_add_u32 s100, s100, s89
	s_addc_u32 s101, s101, 0
	global_load_dword v78, v178, s[100:101] nt
	s_add_u32 s100, s100, s89
	s_addc_u32 s101, s101, 0
	global_load_dword v79, v178, s[100:101] nt
	s_add_u32 s100, s100, s89
	s_addc_u32 s101, s101, 0
	global_load_dword v80, v178, s[100:101] nt
	s_add_u32 s100, s100, s89
	s_addc_u32 s101, s101, 0
	global_load_dword v81, v178, s[100:101] nt
	s_add_u32 s100, s100, s89
	s_addc_u32 s101, s101, 0
	global_load_dword v82, v178, s[100:101] nt
	s_add_u32 s100, s100, s89
	s_addc_u32 s101, s101, 0
	global_load_dword v83, v178, s[100:101] nt
	s_add_u32 s100, s100, s89
	s_addc_u32 s101, s101, 0
	global_load_dword v84, v178, s[100:101] nt
	s_add_u32 s100, s100, s89
	s_addc_u32 s101, s101, 0
	global_load_dword v85, v178, s[100:101] nt
	s_add_u32 s100, s100, s89
	s_addc_u32 s101, s101, 0
	global_load_dword v86, v178, s[100:101] nt
	s_add_u32 s100, s100, s89
	s_addc_u32 s101, s101, 0
	global_load_dword v87, v178, s[100:101] nt
	s_add_u32 s100, s100, s89
	s_addc_u32 s101, s101, 0
	global_load_dword v88, v178, s[100:101] nt
	s_add_u32 s100, s100, s89
	s_addc_u32 s101, s101, 0
	global_load_dword v89, v178, s[100:101] nt
	s_add_u32 s100, s100, s89
	s_addc_u32 s101, s101, 0
	global_load_dword v90, v178, s[100:101] nt
	s_add_u32 s100, s100, s89
	s_addc_u32 s101, s101, 0
	global_load_dword v91, v178, s[100:101] nt
	s_add_u32 s100, s100, s89
	s_addc_u32 s101, s101, 0
	global_load_dword v92, v178, s[100:101] nt
	s_add_u32 s100, s100, s89
	s_addc_u32 s101, s101, 0
	global_load_dword v93, v178, s[100:101] nt
	s_add_u32 s100, s100, s89
	s_addc_u32 s101, s101, 0
	global_load_dword v94, v178, s[100:101] nt
	s_add_u32 s100, s100, s89
	s_addc_u32 s101, s101, 0
	global_load_dword v95, v178, s[100:101] nt
	s_add_u32 s100, s100, s89
	s_addc_u32 s101, s101, 0
	global_load_dword v96, v178, s[100:101] nt
	s_add_u32 s100, s100, s89
	s_addc_u32 s101, s101, 0
	global_load_dword v97, v178, s[100:101] nt
	s_add_u32 s100, s100, s89
	s_addc_u32 s101, s101, 0
	s_waitcnt vmcnt(48)
	v_mul_f32_e32 v34, 0x42000000, v34
	v_mul_f32_e32 v35, 0x42000000, v35
	v_mul_f32_e32 v36, 0x42000000, v36
	v_mul_f32_e32 v37, 0x42000000, v37
	v_mul_f32_e32 v38, 0x42000000, v38
	v_mul_f32_e32 v39, 0x42000000, v39
	v_mul_f32_e32 v40, 0x42000000, v40
	v_mul_f32_e32 v41, 0x42000000, v41
	v_mul_f32_e32 v42, 0x42000000, v42
	v_mul_f32_e32 v43, 0x42000000, v43
	v_mul_f32_e32 v44, 0x42000000, v44
	v_mul_f32_e32 v45, 0x42000000, v45
	v_mul_f32_e32 v46, 0x42000000, v46
	v_mul_f32_e32 v47, 0x42000000, v47
	v_mul_f32_e32 v48, 0x42000000, v48
	v_mul_f32_e32 v49, 0x42000000, v49
	v_cvt_pk_fp8_f32 v154, v34, v35
	v_cvt_pk_fp8_f32 v155, v38, v39
	v_cvt_pk_fp8_f32 v156, v42, v43
	v_cvt_pk_fp8_f32 v157, v46, v47
	v_cvt_pk_fp8_f32 v154, v36, v37 op_sel:[0,0,1]
	v_cvt_pk_fp8_f32 v155, v40, v41 op_sel:[0,0,1]
	v_cvt_pk_fp8_f32 v156, v44, v45 op_sel:[0,0,1]
	v_cvt_pk_fp8_f32 v157, v48, v49 op_sel:[0,0,1]
	s_waitcnt vmcnt(32)
	v_mul_f32_e32 v50, 0x42000000, v50
	v_mul_f32_e32 v51, 0x42000000, v51
	v_mul_f32_e32 v52, 0x42000000, v52
	v_mul_f32_e32 v53, 0x42000000, v53
	v_mul_f32_e32 v54, 0x42000000, v54
	v_mul_f32_e32 v55, 0x42000000, v55
	v_mul_f32_e32 v56, 0x42000000, v56
	v_mul_f32_e32 v57, 0x42000000, v57
	v_mul_f32_e32 v58, 0x42000000, v58
	v_mul_f32_e32 v59, 0x42000000, v59
	v_mul_f32_e32 v60, 0x42000000, v60
	v_mul_f32_e32 v61, 0x42000000, v61
	v_mul_f32_e32 v62, 0x42000000, v62
	v_mul_f32_e32 v63, 0x42000000, v63
	v_mul_f32_e32 v64, 0x42000000, v64
	v_mul_f32_e32 v65, 0x42000000, v65
	v_cvt_pk_fp8_f32 v158, v50, v51
	v_cvt_pk_fp8_f32 v159, v54, v55
	v_cvt_pk_fp8_f32 v160, v58, v59
	v_cvt_pk_fp8_f32 v161, v62, v63
	v_cvt_pk_fp8_f32 v158, v52, v53 op_sel:[0,0,1]
	v_cvt_pk_fp8_f32 v159, v56, v57 op_sel:[0,0,1]
	v_cvt_pk_fp8_f32 v160, v60, v61 op_sel:[0,0,1]
	v_cvt_pk_fp8_f32 v161, v64, v65 op_sel:[0,0,1]
	s_waitcnt vmcnt(16)
	v_mul_f32_e32 v66, 0x42000000, v66
	v_mul_f32_e32 v67, 0x42000000, v67
	v_mul_f32_e32 v68, 0x42000000, v68
	v_mul_f32_e32 v69, 0x42000000, v69
	v_mul_f32_e32 v70, 0x42000000, v70
	v_mul_f32_e32 v71, 0x42000000, v71
	v_mul_f32_e32 v72, 0x42000000, v72
	v_mul_f32_e32 v73, 0x42000000, v73
	v_mul_f32_e32 v74, 0x42000000, v74
	v_mul_f32_e32 v75, 0x42000000, v75
	v_mul_f32_e32 v76, 0x42000000, v76
	v_mul_f32_e32 v77, 0x42000000, v77
	v_mul_f32_e32 v78, 0x42000000, v78
	v_mul_f32_e32 v79, 0x42000000, v79
	v_mul_f32_e32 v80, 0x42000000, v80
	v_mul_f32_e32 v81, 0x42000000, v81
	v_cvt_pk_fp8_f32 v162, v66, v67
	v_cvt_pk_fp8_f32 v163, v70, v71
	v_cvt_pk_fp8_f32 v164, v74, v75
	v_cvt_pk_fp8_f32 v165, v78, v79
	v_cvt_pk_fp8_f32 v162, v68, v69 op_sel:[0,0,1]
	v_cvt_pk_fp8_f32 v163, v72, v73 op_sel:[0,0,1]
	v_cvt_pk_fp8_f32 v164, v76, v77 op_sel:[0,0,1]
	v_cvt_pk_fp8_f32 v165, v80, v81 op_sel:[0,0,1]
	s_waitcnt vmcnt(0)
	v_mul_f32_e32 v82, 0x42000000, v82
	v_mul_f32_e32 v83, 0x42000000, v83
	v_mul_f32_e32 v84, 0x42000000, v84
	v_mul_f32_e32 v85, 0x42000000, v85
	v_mul_f32_e32 v86, 0x42000000, v86
	v_mul_f32_e32 v87, 0x42000000, v87
	v_mul_f32_e32 v88, 0x42000000, v88
	v_mul_f32_e32 v89, 0x42000000, v89
	v_mul_f32_e32 v90, 0x42000000, v90
	v_mul_f32_e32 v91, 0x42000000, v91
	v_mul_f32_e32 v92, 0x42000000, v92
	v_mul_f32_e32 v93, 0x42000000, v93
	v_mul_f32_e32 v94, 0x42000000, v94
	v_mul_f32_e32 v95, 0x42000000, v95
	v_mul_f32_e32 v96, 0x42000000, v96
	v_mul_f32_e32 v97, 0x42000000, v97
	v_cvt_pk_fp8_f32 v166, v82, v83
	v_cvt_pk_fp8_f32 v167, v86, v87
	v_cvt_pk_fp8_f32 v168, v90, v91
	v_cvt_pk_fp8_f32 v169, v94, v95
	v_cvt_pk_fp8_f32 v166, v84, v85 op_sel:[0,0,1]
	v_cvt_pk_fp8_f32 v167, v88, v89 op_sel:[0,0,1]
	v_cvt_pk_fp8_f32 v168, v92, v93 op_sel:[0,0,1]
	v_cvt_pk_fp8_f32 v169, v96, v97 op_sel:[0,0,1]
	s_mov_b32 vcc_lo, 0xaaaaaaaa
	s_mov_b32 vcc_hi, 0xaaaaaaaa
	s_nop 1
	v_cndmask_b32_dpp v170, v154, v158, vcc quad_perm:[1,0,3,2] row_mask:0xf bank_mask:0xf
	v_cndmask_b32_dpp v174, v162, v166, vcc quad_perm:[1,0,3,2] row_mask:0xf bank_mask:0xf
	v_cndmask_b32_dpp v171, v155, v159, vcc quad_perm:[1,0,3,2] row_mask:0xf bank_mask:0xf
	v_cndmask_b32_dpp v175, v163, v167, vcc quad_perm:[1,0,3,2] row_mask:0xf bank_mask:0xf
	v_cndmask_b32_dpp v172, v156, v160, vcc quad_perm:[1,0,3,2] row_mask:0xf bank_mask:0xf
	v_cndmask_b32_dpp v176, v164, v168, vcc quad_perm:[1,0,3,2] row_mask:0xf bank_mask:0xf
	v_cndmask_b32_dpp v173, v157, v161, vcc quad_perm:[1,0,3,2] row_mask:0xf bank_mask:0xf
	v_cndmask_b32_dpp v177, v165, v169, vcc quad_perm:[1,0,3,2] row_mask:0xf bank_mask:0xf
	s_mov_b32 vcc_lo, 0x55555555
	s_mov_b32 vcc_hi, 0x55555555
	s_nop 1
	v_cndmask_b32_dpp v154, v158, v154, vcc quad_perm:[1,0,3,2] row_mask:0xf bank_mask:0xf
	v_cndmask_b32_dpp v162, v166, v162, vcc quad_perm:[1,0,3,2] row_mask:0xf bank_mask:0xf
	v_cndmask_b32_dpp v155, v159, v155, vcc quad_perm:[1,0,3,2] row_mask:0xf bank_mask:0xf
	v_cndmask_b32_dpp v163, v167, v163, vcc quad_perm:[1,0,3,2] row_mask:0xf bank_mask:0xf
	v_cndmask_b32_dpp v156, v160, v156, vcc quad_perm:[1,0,3,2] row_mask:0xf bank_mask:0xf
	v_cndmask_b32_dpp v164, v168, v164, vcc quad_perm:[1,0,3,2] row_mask:0xf bank_mask:0xf
	v_cndmask_b32_dpp v157, v161, v157, vcc quad_perm:[1,0,3,2] row_mask:0xf bank_mask:0xf
	v_cndmask_b32_dpp v165, v169, v165, vcc quad_perm:[1,0,3,2] row_mask:0xf bank_mask:0xf
	s_mov_b32 vcc_lo, 0xcccccccc
	s_mov_b32 vcc_hi, 0xcccccccc
	s_nop 1
	v_cndmask_b32_dpp v158, v154, v162, vcc quad_perm:[2,3,0,1] row_mask:0xf bank_mask:0xf
	v_cndmask_b32_dpp v166, v170, v174, vcc quad_perm:[2,3,0,1] row_mask:0xf bank_mask:0xf
	v_cndmask_b32_dpp v159, v155, v163, vcc quad_perm:[2,3,0,1] row_mask:0xf bank_mask:0xf
	v_cndmask_b32_dpp v167, v171, v175, vcc quad_perm:[2,3,0,1] row_mask:0xf bank_mask:0xf
	v_cndmask_b32_dpp v160, v156, v164, vcc quad_perm:[2,3,0,1] row_mask:0xf bank_mask:0xf
	v_cndmask_b32_dpp v168, v172, v176, vcc quad_perm:[2,3,0,1] row_mask:0xf bank_mask:0xf
	v_cndmask_b32_dpp v161, v157, v165, vcc quad_perm:[2,3,0,1] row_mask:0xf bank_mask:0xf
	v_cndmask_b32_dpp v169, v173, v177, vcc quad_perm:[2,3,0,1] row_mask:0xf bank_mask:0xf
	s_mov_b32 vcc_lo, 0x33333333
	s_mov_b32 vcc_hi, 0x33333333
	s_nop 1
	v_cndmask_b32_dpp v154, v162, v154, vcc quad_perm:[2,3,0,1] row_mask:0xf bank_mask:0xf
	v_cndmask_b32_dpp v170, v174, v170, vcc quad_perm:[2,3,0,1] row_mask:0xf bank_mask:0xf
	v_cndmask_b32_dpp v155, v163, v155, vcc quad_perm:[2,3,0,1] row_mask:0xf bank_mask:0xf
	v_cndmask_b32_dpp v171, v175, v171, vcc quad_perm:[2,3,0,1] row_mask:0xf bank_mask:0xf
	v_cndmask_b32_dpp v156, v164, v156, vcc quad_perm:[2,3,0,1] row_mask:0xf bank_mask:0xf
	v_cndmask_b32_dpp v172, v176, v172, vcc quad_perm:[2,3,0,1] row_mask:0xf bank_mask:0xf
	v_cndmask_b32_dpp v157, v165, v157, vcc quad_perm:[2,3,0,1] row_mask:0xf bank_mask:0xf
	v_cndmask_b32_dpp v173, v177, v173, vcc quad_perm:[2,3,0,1] row_mask:0xf bank_mask:0xf
	global_store_dwordx4 v179, v[154:157], s[82:83] nt
	global_store_dwordx4 v180, v[170:173], s[82:83] nt
	global_store_dwordx4 v181, v[158:161], s[82:83] nt
	global_store_dwordx4 v190, v[166:169], s[82:83] nt
	v_readlane_b32 s2, v239, 0
	s_lshr_b32 s2, s2, 6
	s_sub_i32 s2, s2, 1
	s_mul_i32 s2, s2, 2
	s_mul_i32 s9, s99, 14
	s_add_i32 s2, s2, s9
	s_add_i32 s2, s2, 1
	s_mul_i32 s2, s2, s74
	v_readlane_b32 s9, v239, 23
	s_lshr_b32 s9, s9, 3
	s_add_i32 s2, s2, s9
	s_cmp_gt_u32 s2, 24575
	s_cbranch_scc1 .Lhw_seam0_done
	v_mbcnt_lo_u32_b32 v178, -1, 0
	v_mbcnt_hi_u32_b32 v178, -1, v178
	v_and_b32_e32 v179, 60, v178
	v_lshlrev_b32_e32 v179, 10, v179
	v_and_b32_e32 v180, 3, v178
	v_lshl_or_b32 v179, v180, 4, v179
	v_add_u32_e32 v180, 0x400, v179
	v_add_u32_e32 v181, 0x800, v179
	v_add_u32_e32 v190, 0xc00, v179
	v_lshlrev_b32_e32 v178, 2, v178
	s_cmp_lt_u32 s2, 16384
	s_cbranch_scc0 .Lhw_dn_s0_1
	s_lshr_b32 s9, s2, 9
	s_bfe_u32 s32, s2, 0x40005
	s_and_b32 s53, s2, 31
	s_lshl_b32 s69, s9, 23
	s_lshl_b32 s100, s32, 19
	s_add_i32 s69, s69, s100
	s_lshl_b32 s100, s53, 8
	s_add_i32 s69, s69, s100
	s_lshl_b32 s98, s9, 11
	s_bfe_u32 s100, s53, 0x30001
	s_lshl_b32 s100, s100, 8
	s_add_i32 s98, s98, s100
	s_lshr_b32 s100, s53, 4
	s_lshl_b32 s100, s100, 7
	s_add_i32 s98, s98, s100
	s_and_b32 s100, s53, 1
	s_lshl_b32 s100, s100, 6
	s_add_i32 s98, s98, s100
	s_lshl_b32 s98, s98, 10
	s_lshl_b32 s100, s32, 6
	s_add_i32 s98, s98, s100
	s_add_i32 s98, s98, 0x2000000
	v_readlane_b32 s82, v239, 11
	v_readlane_b32 s83, v239, 12
	s_movk_i32 s89, 8192
	s_branch .Lhw_go_s0_1

.Lhw_go_s0_1:
	s_add_u32 s100, s82, s69
	s_addc_u32 s101, s83, 0
	v_readlane_b32 s82, v239, 44
	v_readlane_b32 s83, v239, 45
	s_add_u32 s82, s82, s98
	s_addc_u32 s83, s83, 0
	global_load_dword v34, v178, s[100:101] nt
	s_add_u32 s100, s100, s89
	s_addc_u32 s101, s101, 0
	global_load_dword v35, v178, s[100:101] nt
	s_add_u32 s100, s100, s89
	s_addc_u32 s101, s101, 0
	global_load_dword v36, v178, s[100:101] nt
	s_add_u32 s100, s100, s89
	s_addc_u32 s101, s101, 0
	global_load_dword v37, v178, s[100:101] nt
	s_add_u32 s100, s100, s89
	s_addc_u32 s101, s101, 0
	global_load_dword v38, v178, s[100:101] nt
	s_add_u32 s100, s100, s89
	s_addc_u32 s101, s101, 0
	global_load_dword v39, v178, s[100:101] nt
	s_add_u32 s100, s100, s89
	s_addc_u32 s101, s101, 0
	global_load_dword v40, v178, s[100:101] nt
	s_add_u32 s100, s100, s89
	s_addc_u32 s101, s101, 0
	global_load_dword v41, v178, s[100:101] nt
	s_add_u32 s100, s100, s89
	s_addc_u32 s101, s101, 0
	global_load_dword v42, v178, s[100:101] nt
	s_add_u32 s100, s100, s89
	s_addc_u32 s101, s101, 0
	global_load_dword v43, v178, s[100:101] nt
	s_add_u32 s100, s100, s89
	s_addc_u32 s101, s101, 0
	global_load_dword v44, v178, s[100:101] nt
	s_add_u32 s100, s100, s89
	s_addc_u32 s101, s101, 0
	global_load_dword v45, v178, s[100:101] nt
	s_add_u32 s100, s100, s89
	s_addc_u32 s101, s101, 0
	global_load_dword v46, v178, s[100:101] nt
	s_add_u32 s100, s100, s89
	s_addc_u32 s101, s101, 0
	global_load_dword v47, v178, s[100:101] nt
	s_add_u32 s100, s100, s89
	s_addc_u32 s101, s101, 0
	global_load_dword v48, v178, s[100:101] nt
	s_add_u32 s100, s100, s89
	s_addc_u32 s101, s101, 0
	global_load_dword v49, v178, s[100:101] nt
	s_add_u32 s100, s100, s89
	s_addc_u32 s101, s101, 0
	global_load_dword v50, v178, s[100:101] nt
	s_add_u32 s100, s100, s89
	s_addc_u32 s101, s101, 0
	global_load_dword v51, v178, s[100:101] nt
	s_add_u32 s100, s100, s89
	s_addc_u32 s101, s101, 0
	global_load_dword v52, v178, s[100:101] nt
	s_add_u32 s100, s100, s89
	s_addc_u32 s101, s101, 0
	global_load_dword v53, v178, s[100:101] nt
	s_add_u32 s100, s100, s89
	s_addc_u32 s101, s101, 0
	global_load_dword v54, v178, s[100:101] nt
	s_add_u32 s100, s100, s89
	s_addc_u32 s101, s101, 0
	global_load_dword v55, v178, s[100:101] nt
	s_add_u32 s100, s100, s89
	s_addc_u32 s101, s101, 0
	global_load_dword v56, v178, s[100:101] nt
	s_add_u32 s100, s100, s89
	s_addc_u32 s101, s101, 0
	global_load_dword v57, v178, s[100:101] nt
	s_add_u32 s100, s100, s89
	s_addc_u32 s101, s101, 0
	global_load_dword v58, v178, s[100:101] nt
	s_add_u32 s100, s100, s89
	s_addc_u32 s101, s101, 0
	global_load_dword v59, v178, s[100:101] nt
	s_add_u32 s100, s100, s89
	s_addc_u32 s101, s101, 0
	global_load_dword v60, v178, s[100:101] nt
	s_add_u32 s100, s100, s89
	s_addc_u32 s101, s101, 0
	global_load_dword v61, v178, s[100:101] nt
	s_add_u32 s100, s100, s89
	s_addc_u32 s101, s101, 0
	global_load_dword v62, v178, s[100:101] nt
	s_add_u32 s100, s100, s89
	s_addc_u32 s101, s101, 0
	global_load_dword v63, v178, s[100:101] nt
	s_add_u32 s100, s100, s89
	s_addc_u32 s101, s101, 0
	global_load_dword v64, v178, s[100:101] nt
	s_add_u32 s100, s100, s89
	s_addc_u32 s101, s101, 0
	global_load_dword v65, v178, s[100:101] nt
	s_add_u32 s100, s100, s89
	s_addc_u32 s101, s101, 0
	global_load_dword v66, v178, s[100:101] nt
	s_add_u32 s100, s100, s89
	s_addc_u32 s101, s101, 0
	global_load_dword v67, v178, s[100:101] nt
	s_add_u32 s100, s100, s89
	s_addc_u32 s101, s101, 0
	global_load_dword v68, v178, s[100:101] nt
	s_add_u32 s100, s100, s89
	s_addc_u32 s101, s101, 0
	global_load_dword v69, v178, s[100:101] nt
	s_add_u32 s100, s100, s89
	s_addc_u32 s101, s101, 0
	global_load_dword v70, v178, s[100:101] nt
	s_add_u32 s100, s100, s89
	s_addc_u32 s101, s101, 0
	global_load_dword v71, v178, s[100:101] nt
	s_add_u32 s100, s100, s89
	s_addc_u32 s101, s101, 0
	global_load_dword v72, v178, s[100:101] nt
	s_add_u32 s100, s100, s89
	s_addc_u32 s101, s101, 0
	global_load_dword v73, v178, s[100:101] nt
	s_add_u32 s100, s100, s89
	s_addc_u32 s101, s101, 0
	global_load_dword v74, v178, s[100:101] nt
	s_add_u32 s100, s100, s89
	s_addc_u32 s101, s101, 0
	global_load_dword v75, v178, s[100:101] nt
	s_add_u32 s100, s100, s89
	s_addc_u32 s101, s101, 0
	global_load_dword v76, v178, s[100:101] nt
	s_add_u32 s100, s100, s89
	s_addc_u32 s101, s101, 0
	global_load_dword v77, v178, s[100:101] nt
	s_add_u32 s100, s100, s89
	s_addc_u32 s101, s101, 0
	global_load_dword v78, v178, s[100:101] nt
	s_add_u32 s100, s100, s89
	s_addc_u32 s101, s101, 0
	global_load_dword v79, v178, s[100:101] nt
	s_add_u32 s100, s100, s89
	s_addc_u32 s101, s101, 0
	global_load_dword v80, v178, s[100:101] nt
	s_add_u32 s100, s100, s89
	s_addc_u32 s101, s101, 0
	global_load_dword v81, v178, s[100:101] nt
	s_add_u32 s100, s100, s89
	s_addc_u32 s101, s101, 0
	global_load_dword v82, v178, s[100:101] nt
	s_add_u32 s100, s100, s89
	s_addc_u32 s101, s101, 0
	global_load_dword v83, v178, s[100:101] nt
	s_add_u32 s100, s100, s89
	s_addc_u32 s101, s101, 0
	global_load_dword v84, v178, s[100:101] nt
	s_add_u32 s100, s100, s89
	s_addc_u32 s101, s101, 0
	global_load_dword v85, v178, s[100:101] nt
	s_add_u32 s100, s100, s89
	s_addc_u32 s101, s101, 0
	global_load_dword v86, v178, s[100:101] nt
	s_add_u32 s100, s100, s89
	s_addc_u32 s101, s101, 0
	global_load_dword v87, v178, s[100:101] nt
	s_add_u32 s100, s100, s89
	s_addc_u32 s101, s101, 0
	global_load_dword v88, v178, s[100:101] nt
	s_add_u32 s100, s100, s89
	s_addc_u32 s101, s101, 0
	global_load_dword v89, v178, s[100:101] nt
	s_add_u32 s100, s100, s89
	s_addc_u32 s101, s101, 0
	global_load_dword v90, v178, s[100:101] nt
	s_add_u32 s100, s100, s89
	s_addc_u32 s101, s101, 0
	global_load_dword v91, v178, s[100:101] nt
	s_add_u32 s100, s100, s89
	s_addc_u32 s101, s101, 0
	global_load_dword v92, v178, s[100:101] nt
	s_add_u32 s100, s100, s89
	s_addc_u32 s101, s101, 0
	global_load_dword v93, v178, s[100:101] nt
	s_add_u32 s100, s100, s89
	s_addc_u32 s101, s101, 0
	global_load_dword v94, v178, s[100:101] nt
	s_add_u32 s100, s100, s89
	s_addc_u32 s101, s101, 0
	global_load_dword v95, v178, s[100:101] nt
	s_add_u32 s100, s100, s89
	s_addc_u32 s101, s101, 0
	global_load_dword v96, v178, s[100:101] nt
	s_add_u32 s100, s100, s89
	s_addc_u32 s101, s101, 0
	global_load_dword v97, v178, s[100:101] nt
	s_add_u32 s100, s100, s89
	s_addc_u32 s101, s101, 0
	s_waitcnt vmcnt(48)
	v_mul_f32_e32 v34, 0x42000000, v34
	v_mul_f32_e32 v35, 0x42000000, v35
	v_mul_f32_e32 v36, 0x42000000, v36
	v_mul_f32_e32 v37, 0x42000000, v37
	v_mul_f32_e32 v38, 0x42000000, v38
	v_mul_f32_e32 v39, 0x42000000, v39
	v_mul_f32_e32 v40, 0x42000000, v40
	v_mul_f32_e32 v41, 0x42000000, v41
	v_mul_f32_e32 v42, 0x42000000, v42
	v_mul_f32_e32 v43, 0x42000000, v43
	v_mul_f32_e32 v44, 0x42000000, v44
	v_mul_f32_e32 v45, 0x42000000, v45
	v_mul_f32_e32 v46, 0x42000000, v46
	v_mul_f32_e32 v47, 0x42000000, v47
	v_mul_f32_e32 v48, 0x42000000, v48
	v_mul_f32_e32 v49, 0x42000000, v49
	v_cvt_pk_fp8_f32 v154, v34, v35
	v_cvt_pk_fp8_f32 v155, v38, v39
	v_cvt_pk_fp8_f32 v156, v42, v43
	v_cvt_pk_fp8_f32 v157, v46, v47
	v_cvt_pk_fp8_f32 v154, v36, v37 op_sel:[0,0,1]
	v_cvt_pk_fp8_f32 v155, v40, v41 op_sel:[0,0,1]
	v_cvt_pk_fp8_f32 v156, v44, v45 op_sel:[0,0,1]
	v_cvt_pk_fp8_f32 v157, v48, v49 op_sel:[0,0,1]
	s_waitcnt vmcnt(32)
	v_mul_f32_e32 v50, 0x42000000, v50
	v_mul_f32_e32 v51, 0x42000000, v51
	v_mul_f32_e32 v52, 0x42000000, v52
	v_mul_f32_e32 v53, 0x42000000, v53
	v_mul_f32_e32 v54, 0x42000000, v54
	v_mul_f32_e32 v55, 0x42000000, v55
	v_mul_f32_e32 v56, 0x42000000, v56
	v_mul_f32_e32 v57, 0x42000000, v57
	v_mul_f32_e32 v58, 0x42000000, v58
	v_mul_f32_e32 v59, 0x42000000, v59
	v_mul_f32_e32 v60, 0x42000000, v60
	v_mul_f32_e32 v61, 0x42000000, v61
	v_mul_f32_e32 v62, 0x42000000, v62
	v_mul_f32_e32 v63, 0x42000000, v63
	v_mul_f32_e32 v64, 0x42000000, v64
	v_mul_f32_e32 v65, 0x42000000, v65
	v_cvt_pk_fp8_f32 v158, v50, v51
	v_cvt_pk_fp8_f32 v159, v54, v55
	v_cvt_pk_fp8_f32 v160, v58, v59
	v_cvt_pk_fp8_f32 v161, v62, v63
	v_cvt_pk_fp8_f32 v158, v52, v53 op_sel:[0,0,1]
	v_cvt_pk_fp8_f32 v159, v56, v57 op_sel:[0,0,1]
	v_cvt_pk_fp8_f32 v160, v60, v61 op_sel:[0,0,1]
	v_cvt_pk_fp8_f32 v161, v64, v65 op_sel:[0,0,1]
	s_waitcnt vmcnt(16)
	v_mul_f32_e32 v66, 0x42000000, v66
	v_mul_f32_e32 v67, 0x42000000, v67
	v_mul_f32_e32 v68, 0x42000000, v68
	v_mul_f32_e32 v69, 0x42000000, v69
	v_mul_f32_e32 v70, 0x42000000, v70
	v_mul_f32_e32 v71, 0x42000000, v71
	v_mul_f32_e32 v72, 0x42000000, v72
	v_mul_f32_e32 v73, 0x42000000, v73
	v_mul_f32_e32 v74, 0x42000000, v74
	v_mul_f32_e32 v75, 0x42000000, v75
	v_mul_f32_e32 v76, 0x42000000, v76
	v_mul_f32_e32 v77, 0x42000000, v77
	v_mul_f32_e32 v78, 0x42000000, v78
	v_mul_f32_e32 v79, 0x42000000, v79
	v_mul_f32_e32 v80, 0x42000000, v80
	v_mul_f32_e32 v81, 0x42000000, v81
	v_cvt_pk_fp8_f32 v162, v66, v67
	v_cvt_pk_fp8_f32 v163, v70, v71
	v_cvt_pk_fp8_f32 v164, v74, v75
	v_cvt_pk_fp8_f32 v165, v78, v79
	v_cvt_pk_fp8_f32 v162, v68, v69 op_sel:[0,0,1]
	v_cvt_pk_fp8_f32 v163, v72, v73 op_sel:[0,0,1]
	v_cvt_pk_fp8_f32 v164, v76, v77 op_sel:[0,0,1]
	v_cvt_pk_fp8_f32 v165, v80, v81 op_sel:[0,0,1]
	s_waitcnt vmcnt(0)
	v_mul_f32_e32 v82, 0x42000000, v82
	v_mul_f32_e32 v83, 0x42000000, v83
	v_mul_f32_e32 v84, 0x42000000, v84
	v_mul_f32_e32 v85, 0x42000000, v85
	v_mul_f32_e32 v86, 0x42000000, v86
	v_mul_f32_e32 v87, 0x42000000, v87
	v_mul_f32_e32 v88, 0x42000000, v88
	v_mul_f32_e32 v89, 0x42000000, v89
	v_mul_f32_e32 v90, 0x42000000, v90
	v_mul_f32_e32 v91, 0x42000000, v91
	v_mul_f32_e32 v92, 0x42000000, v92
	v_mul_f32_e32 v93, 0x42000000, v93
	v_mul_f32_e32 v94, 0x42000000, v94
	v_mul_f32_e32 v95, 0x42000000, v95
	v_mul_f32_e32 v96, 0x42000000, v96
	v_mul_f32_e32 v97, 0x42000000, v97
	v_cvt_pk_fp8_f32 v166, v82, v83
	v_cvt_pk_fp8_f32 v167, v86, v87
	v_cvt_pk_fp8_f32 v168, v90, v91
	v_cvt_pk_fp8_f32 v169, v94, v95
	v_cvt_pk_fp8_f32 v166, v84, v85 op_sel:[0,0,1]
	v_cvt_pk_fp8_f32 v167, v88, v89 op_sel:[0,0,1]
	v_cvt_pk_fp8_f32 v168, v92, v93 op_sel:[0,0,1]
	v_cvt_pk_fp8_f32 v169, v96, v97 op_sel:[0,0,1]
	s_mov_b32 vcc_lo, 0xaaaaaaaa
	s_mov_b32 vcc_hi, 0xaaaaaaaa
	s_nop 1
	v_cndmask_b32_dpp v170, v154, v158, vcc quad_perm:[1,0,3,2] row_mask:0xf bank_mask:0xf
	v_cndmask_b32_dpp v174, v162, v166, vcc quad_perm:[1,0,3,2] row_mask:0xf bank_mask:0xf
	v_cndmask_b32_dpp v171, v155, v159, vcc quad_perm:[1,0,3,2] row_mask:0xf bank_mask:0xf
	v_cndmask_b32_dpp v175, v163, v167, vcc quad_perm:[1,0,3,2] row_mask:0xf bank_mask:0xf
	v_cndmask_b32_dpp v172, v156, v160, vcc quad_perm:[1,0,3,2] row_mask:0xf bank_mask:0xf
	v_cndmask_b32_dpp v176, v164, v168, vcc quad_perm:[1,0,3,2] row_mask:0xf bank_mask:0xf
	v_cndmask_b32_dpp v173, v157, v161, vcc quad_perm:[1,0,3,2] row_mask:0xf bank_mask:0xf
	v_cndmask_b32_dpp v177, v165, v169, vcc quad_perm:[1,0,3,2] row_mask:0xf bank_mask:0xf
	s_mov_b32 vcc_lo, 0x55555555
	s_mov_b32 vcc_hi, 0x55555555
	s_nop 1
	v_cndmask_b32_dpp v154, v158, v154, vcc quad_perm:[1,0,3,2] row_mask:0xf bank_mask:0xf
	v_cndmask_b32_dpp v162, v166, v162, vcc quad_perm:[1,0,3,2] row_mask:0xf bank_mask:0xf
	v_cndmask_b32_dpp v155, v159, v155, vcc quad_perm:[1,0,3,2] row_mask:0xf bank_mask:0xf
	v_cndmask_b32_dpp v163, v167, v163, vcc quad_perm:[1,0,3,2] row_mask:0xf bank_mask:0xf
	v_cndmask_b32_dpp v156, v160, v156, vcc quad_perm:[1,0,3,2] row_mask:0xf bank_mask:0xf
	v_cndmask_b32_dpp v164, v168, v164, vcc quad_perm:[1,0,3,2] row_mask:0xf bank_mask:0xf
	v_cndmask_b32_dpp v157, v161, v157, vcc quad_perm:[1,0,3,2] row_mask:0xf bank_mask:0xf
	v_cndmask_b32_dpp v165, v169, v165, vcc quad_perm:[1,0,3,2] row_mask:0xf bank_mask:0xf
	s_mov_b32 vcc_lo, 0xcccccccc
	s_mov_b32 vcc_hi, 0xcccccccc
	s_nop 1
	v_cndmask_b32_dpp v158, v154, v162, vcc quad_perm:[2,3,0,1] row_mask:0xf bank_mask:0xf
	v_cndmask_b32_dpp v166, v170, v174, vcc quad_perm:[2,3,0,1] row_mask:0xf bank_mask:0xf
	v_cndmask_b32_dpp v159, v155, v163, vcc quad_perm:[2,3,0,1] row_mask:0xf bank_mask:0xf
	v_cndmask_b32_dpp v167, v171, v175, vcc quad_perm:[2,3,0,1] row_mask:0xf bank_mask:0xf
	v_cndmask_b32_dpp v160, v156, v164, vcc quad_perm:[2,3,0,1] row_mask:0xf bank_mask:0xf
	v_cndmask_b32_dpp v168, v172, v176, vcc quad_perm:[2,3,0,1] row_mask:0xf bank_mask:0xf
	v_cndmask_b32_dpp v161, v157, v165, vcc quad_perm:[2,3,0,1] row_mask:0xf bank_mask:0xf
	v_cndmask_b32_dpp v169, v173, v177, vcc quad_perm:[2,3,0,1] row_mask:0xf bank_mask:0xf
	s_mov_b32 vcc_lo, 0x33333333
	s_mov_b32 vcc_hi, 0x33333333
	s_nop 1
	v_cndmask_b32_dpp v154, v162, v154, vcc quad_perm:[2,3,0,1] row_mask:0xf bank_mask:0xf
	v_cndmask_b32_dpp v170, v174, v170, vcc quad_perm:[2,3,0,1] row_mask:0xf bank_mask:0xf
	v_cndmask_b32_dpp v155, v163, v155, vcc quad_perm:[2,3,0,1] row_mask:0xf bank_mask:0xf
	v_cndmask_b32_dpp v171, v175, v171, vcc quad_perm:[2,3,0,1] row_mask:0xf bank_mask:0xf
	v_cndmask_b32_dpp v156, v164, v156, vcc quad_perm:[2,3,0,1] row_mask:0xf bank_mask:0xf
	v_cndmask_b32_dpp v172, v176, v172, vcc quad_perm:[2,3,0,1] row_mask:0xf bank_mask:0xf
	v_cndmask_b32_dpp v157, v165, v157, vcc quad_perm:[2,3,0,1] row_mask:0xf bank_mask:0xf
	v_cndmask_b32_dpp v173, v177, v173, vcc quad_perm:[2,3,0,1] row_mask:0xf bank_mask:0xf
	global_store_dwordx4 v179, v[154:157], s[82:83] nt
	global_store_dwordx4 v180, v[170:173], s[82:83] nt
	global_store_dwordx4 v181, v[158:161], s[82:83] nt
	global_store_dwordx4 v190, v[166:169], s[82:83] nt
.Lhw_seam0_done:
	s_add_i32 s99, s99, 1
	s_branch .LBB0_107
